# grid barrier: agent-scope acquire issued at arrival (before polling) instead of after the release
# speedup vs baseline: 1.0274x; 1.0122x over previous
.LBB0_100:
	s_or_b64 exec, exec, s[12:13]
	v_cvt_f32_u32_e32 v5, v3
	s_waitcnt vmcnt(0)
	v_readfirstlane_b32 s10, v4
	v_sub_u32_e32 v4, 0, v3
	v_rcp_iflag_f32_e32 v5, v5
	v_add_u32_e32 v6, s10, v2
	v_mul_f32_e32 v5, 0x4f7ffffe, v5
	v_cvt_u32_f32_e32 v5, v5
	v_mul_lo_u32 v2, v4, v5
	v_mul_hi_u32 v2, v5, v2
	v_add_u32_e32 v2, v5, v2
	v_mul_hi_u32 v2, v6, v2
	v_mul_lo_u32 v4, v2, v3
	v_sub_u32_e32 v4, v6, v4
	v_add_u32_e32 v5, 1, v2
	v_cmp_ge_u32_e32 vcc, v4, v3
	s_nop 1
	v_cndmask_b32_e32 v2, v2, v5, vcc
	v_sub_u32_e32 v5, v4, v3
	v_cndmask_b32_e32 v4, v4, v5, vcc
	v_add_u32_e32 v5, 1, v2
	v_cmp_ge_u32_e32 vcc, v4, v3
	v_add_u32_e32 v4, 1, v6
	s_nop 0
	v_cndmask_b32_e32 v2, v2, v5, vcc
	v_mul_lo_u32 v5, v3, v2
	v_add_u32_e32 v3, v5, v3
	v_cmp_ne_u32_e32 vcc, v4, v3
	s_and_saveexec_b64 s[10:11], vcc
	s_xor_b64 s[10:11], exec, s[10:11]
	s_cbranch_execz .LBB0_114
	s_waitcnt lgkmcnt(0)
	v_mov_b32_e32 v1, 0x2000
	buffer_inv sc1
	global_load_dword v1, v1, s[4:5] offset:1024 sc1
	s_add_u32 s14, s4, 0x2400
	s_addc_u32 s15, s5, 0
	s_waitcnt vmcnt(0)
	v_cmp_eq_u32_e32 vcc, v1, v2
	s_and_saveexec_b64 s[12:13], vcc
	s_cbranch_execz .LBB0_113
	s_mov_b32 s26, 1
	s_mov_b64 s[16:17], 0
	v_mov_b32_e32 v1, 0
	s_branch .LBB0_104

.LBB0_113:
	s_or_b64 exec, exec, s[12:13]
	s_waitcnt vmcnt(0)
	s_waitcnt vmcnt(0)
.LBB0_114:
	s_andn2_saveexec_b64 s[10:11], s[10:11]
	s_cbranch_execz .LBB0_134
	s_mov_b64 s[10:11], exec
	buffer_wbl2 sc1
	s_waitcnt lgkmcnt(0)
	s_waitcnt vmcnt(0)
	buffer_inv sc1
	v_mbcnt_lo_u32_b32 v2, s10, 0
	v_mbcnt_hi_u32_b32 v2, s11, v2
	v_cmp_eq_u32_e32 vcc, 0, v2
	s_and_saveexec_b64 s[12:13], vcc
	s_cbranch_execz .LBB0_117
	s_bcnt1_i32_b64 s10, s[10:11]
	v_mov_b32_e32 v3, 0x3000
	v_mov_b32_e32 v4, s10
	global_atomic_add v3, v3, v4, s[86:87] offset:1024 sc0

.LBB0_131:
	s_or_b64 exec, exec, s[10:11]
	s_mov_b64 s[10:11], exec
	v_mbcnt_lo_u32_b32 v1, s10, 0
	v_mbcnt_hi_u32_b32 v1, s11, v1
	v_cmp_eq_u32_e32 vcc, 0, v1
	s_waitcnt vmcnt(0)
	s_and_saveexec_b64 s[12:13], vcc
	s_cbranch_execz .LBB0_133
	s_bcnt1_i32_b64 s10, s[10:11]
	v_mov_b32_e32 v1, 0x2000
	v_mov_b32_e32 v2, s10
	global_atomic_add v1, v2, s[4:5] offset:1024

.LBB0_1259:
	s_or_b64 exec, exec, s[8:9]
	v_cvt_f32_u32_e32 v5, v3
	s_waitcnt vmcnt(0)
	v_readfirstlane_b32 s3, v4
	v_sub_u32_e32 v4, 0, v3
	v_rcp_iflag_f32_e32 v5, v5
	v_add_u32_e32 v6, s3, v2
	v_mul_f32_e32 v5, 0x4f7ffffe, v5
	v_cvt_u32_f32_e32 v5, v5
	v_mul_lo_u32 v2, v4, v5
	v_mul_hi_u32 v2, v5, v2
	v_add_u32_e32 v2, v5, v2
	v_mul_hi_u32 v2, v6, v2
	v_mul_lo_u32 v4, v2, v3
	v_sub_u32_e32 v4, v6, v4
	v_add_u32_e32 v5, 1, v2
	v_cmp_ge_u32_e32 vcc, v4, v3
	s_nop 1
	v_cndmask_b32_e32 v2, v2, v5, vcc
	v_sub_u32_e32 v5, v4, v3
	v_cndmask_b32_e32 v4, v4, v5, vcc
	v_add_u32_e32 v5, 1, v2
	v_cmp_ge_u32_e32 vcc, v4, v3
	v_add_u32_e32 v4, 1, v6
	s_nop 0
	v_cndmask_b32_e32 v2, v2, v5, vcc
	v_mul_lo_u32 v5, v3, v2
	v_add_u32_e32 v3, v5, v3
	v_cmp_ne_u32_e32 vcc, v4, v3
	s_and_saveexec_b64 s[6:7], vcc
	s_xor_b64 s[6:7], exec, s[6:7]
	s_cbranch_execz .LBB0_1273
	s_waitcnt lgkmcnt(0)
	v_mov_b32_e32 v1, 0x2000
	buffer_inv sc1
	global_load_dword v1, v1, s[4:5] offset:1024 sc1
	s_add_u32 s10, s4, 0x2400
	s_addc_u32 s11, s5, 0
	s_waitcnt vmcnt(0)
	v_cmp_eq_u32_e32 vcc, v1, v2
	s_and_saveexec_b64 s[8:9], vcc
	s_cbranch_execz .LBB0_1272
	s_mov_b32 s3, 1
	s_mov_b64 s[12:13], 0
	v_mov_b32_e32 v1, 0
	s_branch .LBB0_1263

.LBB0_1272:
	s_or_b64 exec, exec, s[8:9]
	s_waitcnt vmcnt(0)
	s_waitcnt vmcnt(0)
.LBB0_1273:
	s_andn2_saveexec_b64 s[6:7], s[6:7]
	s_cbranch_execz .LBB0_1293
	s_mov_b64 s[6:7], exec
	buffer_wbl2 sc1
	s_waitcnt lgkmcnt(0)
	s_waitcnt vmcnt(0)
	buffer_inv sc1
	v_mbcnt_lo_u32_b32 v2, s6, 0
	v_mbcnt_hi_u32_b32 v2, s7, v2
	v_cmp_eq_u32_e32 vcc, 0, v2
	s_and_saveexec_b64 s[8:9], vcc
	s_cbranch_execz .LBB0_1276
	s_bcnt1_i32_b64 s3, s[6:7]
	v_mov_b32_e32 v3, 0x3000
	v_mov_b32_e32 v4, s3
	global_atomic_add v3, v3, v4, s[86:87] offset:1024 sc0

.LBB0_1290:
	s_or_b64 exec, exec, s[6:7]
	s_mov_b64 s[6:7], exec
	v_mbcnt_lo_u32_b32 v1, s6, 0
	v_mbcnt_hi_u32_b32 v1, s7, v1
	v_cmp_eq_u32_e32 vcc, 0, v1
	s_waitcnt vmcnt(0)
	s_and_saveexec_b64 s[8:9], vcc
	s_cbranch_execz .LBB0_1292
	s_bcnt1_i32_b64 s3, s[6:7]
	v_mov_b32_e32 v1, 0x2000
	v_mov_b32_e32 v2, s3
	global_atomic_add v1, v2, s[4:5] offset:1024
